# in-projection and expert-down GEMM epilogue stores written through (sc1); L2 writeback dropped from the two barriers that follow them
# baseline (speedup 1.0000x reference)
; __device__ __forceinline__ unsigned cvt_pk_bf16(float lo, float hi) { unsigned r; asm volatile("v_cvt_pk_bf16_f32 %0, %1, %2" : "=v"(r) : "v"(lo), "v"(hi)); return r; }
;     __device__ __forceinline__ void operator()(const f32x4 (&acc)[2][2][4][2], const Unit& u, int wr, int wc, int fr, int fq) const {
;     ...
;                 for (int m = 0; m < 4; ++m) { bf16_t* rowp = P + (size_t)(row0 + ai * HALF + m * 16) * 3328 + col0;
; #pragma unroll
;                     for (int bj = 0; bj < 2; ++bj) { const f32x4 v0 = acc[ai][bj][m][0], v1 = acc[ai][bj][m][1];
;                         u32x4 w; w.x = cvt_pk_bf16(v0[0], v0[1]); w.y = cvt_pk_bf16(v0[2], v0[3]); w.z = cvt_pk_bf16(v1[0], v1[1]); w.w = cvt_pk_bf16(v1[2], v1[3]);
;                         *(u32x4*)(rowp + bj * HALF) = w; } }
.LBB0_768:
	v_lshl_or_b32 v148, s72, 8, v151
	v_ashrrev_i32_e32 v149, 31, v148
	v_mov_b64_e32 v[146:147], s[6:7]
	v_mad_i64_i32 v[154:155], s[20:21], v144, s33, v[146:147]
	v_lshlrev_b64 v[148:149], 1, v[148:149]
	v_lshl_add_u64 v[154:155], v[154:155], 0, v[148:149]
	v_or_b32_e32 v0, 16, v144
	v_cvt_pk_bf16_f32 v128, v128, v129
	v_cvt_pk_bf16_f32 v129, v130, v131
	v_cvt_pk_bf16_f32 v130, v124, v125
	v_cvt_pk_bf16_f32 v131, v126, v127
	global_store_dwordx4 v[154:155], v[128:131], off sc1
	v_cvt_pk_bf16_f32 v116, v116, v117
	v_cvt_pk_bf16_f32 v117, v118, v119
	v_cvt_pk_bf16_f32 v118, v108, v109
	v_mad_i64_i32 v[108:109], s[20:21], v0, s33, v[146:147]
	v_cvt_pk_bf16_f32 v119, v110, v111
	global_store_dwordx4 v[154:155], v[116:119], off offset:256 sc1
	v_or_b32_e32 v0, 32, v144
	s_nop 0
	v_lshl_add_u64 v[116:117], v[108:109], 0, v[148:149]
	v_cvt_pk_bf16_f32 v108, v120, v121
	v_cvt_pk_bf16_f32 v109, v122, v123
	v_cvt_pk_bf16_f32 v110, v112, v113
	v_cvt_pk_bf16_f32 v111, v114, v115
	global_store_dwordx4 v[116:117], v[108:111], off sc1
	v_cvt_pk_bf16_f32 v100, v100, v101
	v_cvt_pk_bf16_f32 v101, v102, v103
	v_cvt_pk_bf16_f32 v102, v92, v93
	v_mad_i64_i32 v[92:93], s[20:21], v0, s33, v[146:147]
	v_cvt_pk_bf16_f32 v103, v94, v95
	global_store_dwordx4 v[116:117], v[100:103], off offset:256 sc1
	v_or_b32_e32 v0, 48, v144
	s_nop 0
	v_lshl_add_u64 v[100:101], v[92:93], 0, v[148:149]
	v_cvt_pk_bf16_f32 v92, v104, v105
	v_cvt_pk_bf16_f32 v93, v106, v107
	v_cvt_pk_bf16_f32 v94, v96, v97
	v_cvt_pk_bf16_f32 v95, v98, v99
	global_store_dwordx4 v[100:101], v[92:95], off sc1
	v_cvt_pk_bf16_f32 v84, v84, v85
	v_cvt_pk_bf16_f32 v85, v86, v87
	v_cvt_pk_bf16_f32 v86, v76, v77
	v_mad_i64_i32 v[76:77], s[20:21], v0, s33, v[146:147]
	v_cvt_pk_bf16_f32 v87, v78, v79
	global_store_dwordx4 v[100:101], v[84:87], off offset:256 sc1
	v_add_u32_e32 v0, 0x80, v144
	s_nop 0
	v_lshl_add_u64 v[84:85], v[76:77], 0, v[148:149]
	v_cvt_pk_bf16_f32 v76, v88, v89
	v_cvt_pk_bf16_f32 v77, v90, v91
	v_cvt_pk_bf16_f32 v78, v80, v81
	v_cvt_pk_bf16_f32 v79, v82, v83
	global_store_dwordx4 v[84:85], v[76:79], off sc1
	v_cvt_pk_bf16_f32 v72, v72, v73
	v_cvt_pk_bf16_f32 v73, v74, v75
	v_cvt_pk_bf16_f32 v74, v68, v69
	v_mad_i64_i32 v[68:69], s[20:21], v0, s33, v[146:147]
	v_lshl_add_u64 v[68:69], v[68:69], 0, v[148:149]
	v_add_u32_e32 v0, 0x90, v144
	v_cvt_pk_bf16_f32 v75, v70, v71
	global_store_dwordx4 v[84:85], v[72:75], off offset:256 sc1
	v_cvt_pk_bf16_f32 v64, v64, v65
	v_cvt_pk_bf16_f32 v65, v66, v67
	v_cvt_pk_bf16_f32 v66, v60, v61
	v_cvt_pk_bf16_f32 v67, v62, v63
	global_store_dwordx4 v[68:69], v[64:67], off sc1
	v_cvt_pk_bf16_f32 v52, v52, v53
	v_cvt_pk_bf16_f32 v53, v54, v55
	v_cvt_pk_bf16_f32 v54, v44, v45
	v_mad_i64_i32 v[44:45], s[20:21], v0, s33, v[146:147]
	v_cvt_pk_bf16_f32 v55, v46, v47
	global_store_dwordx4 v[68:69], v[52:55], off offset:256 sc1
	v_add_u32_e32 v0, 0xa0, v144
	s_nop 0
	v_lshl_add_u64 v[52:53], v[44:45], 0, v[148:149]
	v_cvt_pk_bf16_f32 v44, v56, v57
	v_cvt_pk_bf16_f32 v45, v58, v59
	v_cvt_pk_bf16_f32 v46, v48, v49
	v_cvt_pk_bf16_f32 v47, v50, v51
	global_store_dwordx4 v[52:53], v[44:47], off sc1
	v_cvt_pk_bf16_f32 v36, v36, v37
	v_cvt_pk_bf16_f32 v37, v38, v39
	v_cvt_pk_bf16_f32 v38, v28, v29
	v_mad_i64_i32 v[28:29], s[20:21], v0, s33, v[146:147]
	v_cvt_pk_bf16_f32 v39, v30, v31
	global_store_dwordx4 v[52:53], v[36:39], off offset:256 sc1
	v_add_u32_e32 v0, 0xb0, v144
	s_nop 0
	v_lshl_add_u64 v[36:37], v[28:29], 0, v[148:149]
	v_cvt_pk_bf16_f32 v28, v40, v41
	v_cvt_pk_bf16_f32 v29, v42, v43
	v_cvt_pk_bf16_f32 v30, v32, v33
	v_cvt_pk_bf16_f32 v31, v34, v35
	global_store_dwordx4 v[36:37], v[28:31], off sc1
	v_cvt_pk_bf16_f32 v20, v20, v21
	v_cvt_pk_bf16_f32 v21, v22, v23
	v_cvt_pk_bf16_f32 v22, v12, v13
	v_mad_i64_i32 v[12:13], s[20:21], v0, s33, v[146:147]
	v_cvt_pk_bf16_f32 v23, v14, v15
	global_store_dwordx4 v[36:37], v[20:23], off offset:256 sc1
	s_nop 1
	v_lshl_add_u64 v[20:21], v[12:13], 0, v[148:149]
	v_cvt_pk_bf16_f32 v12, v24, v25
	v_cvt_pk_bf16_f32 v13, v26, v27
	v_cvt_pk_bf16_f32 v14, v16, v17
	v_cvt_pk_bf16_f32 v15, v18, v19
	global_store_dwordx4 v[20:21], v[12:15], off sc1
	v_cvt_pk_bf16_f32 v8, v8, v9
	v_cvt_pk_bf16_f32 v9, v10, v11
	v_cvt_pk_bf16_f32 v10, v4, v5
	v_cvt_pk_bf16_f32 v11, v6, v7
	global_store_dwordx4 v[20:21], v[8:11], off offset:256 sc1
	s_andn2_b64 vcc, exec, s[2:3]
	s_mov_b64 s[2:3], -1
	s_cbranch_vccnz .LBB0_760
	s_branch .LBB0_774

;     __device__ __forceinline__ void operator()(const f32x4 (&acc)[2][2][4][2], const Unit& u, int wr, int wc, int fr, int fq) const {
;     ...
;         } else if (wc == 0 && fq < 2) {
; #pragma unroll
;             for (int ai = 0; ai < 2; ++ai)
; #pragma unroll
;                 for (int m = 0; m < 4; ++m) { float* gp = G + (size_t)(row0 + ai * HALF + m * 16) * 16 + 8 * fq;
;                     *(f32x4*)(gp) = acc[ai][0][m][0]; *(f32x4*)(gp + 4) = acc[ai][0][m][1]; }
.LBB0_770:
	s_and_saveexec_b64 s[20:21], s[12:13]
	s_cbranch_execz .LBB0_772
	v_or_b32_e32 v148, 16, v144
	v_ashrrev_i32_e32 v145, 31, v144
	v_ashrrev_i32_e32 v149, 31, v148
	v_lshlrev_b64 v[146:147], 6, v[144:145]
	v_lshlrev_b64 v[148:149], 6, v[148:149]
	v_lshl_add_u64 v[146:147], v[138:139], 0, v[146:147]
	v_lshl_add_u64 v[148:149], v[138:139], 0, v[148:149]
	global_store_dwordx4 v[146:147], v[128:131], off sc1
	global_store_dwordx4 v[146:147], v[124:127], off offset:16 sc1
	global_store_dwordx4 v[148:149], v[120:123], off sc1
	global_store_dwordx4 v[148:149], v[112:115], off offset:16 sc1
	v_or_b32_e32 v148, 32, v144
	v_ashrrev_i32_e32 v149, 31, v148
	v_lshlrev_b64 v[148:149], 6, v[148:149]
	v_lshl_add_u64 v[148:149], v[138:139], 0, v[148:149]
	global_store_dwordx4 v[148:149], v[104:107], off sc1
	global_store_dwordx4 v[148:149], v[96:99], off offset:16 sc1
	v_or_b32_e32 v148, 48, v144
	v_ashrrev_i32_e32 v149, 31, v148
	v_lshlrev_b64 v[148:149], 6, v[148:149]
	v_lshl_add_u64 v[148:149], v[138:139], 0, v[148:149]
	s_mov_b64 s[22:23], 0x2000
	v_add_co_u32_e32 v154, vcc, 0x2000, v146
	global_store_dwordx4 v[148:149], v[88:91], off sc1
	global_store_dwordx4 v[148:149], v[80:83], off offset:16 sc1
	v_lshl_add_u64 v[148:149], v[146:147], 0, s[22:23]
	v_addc_co_u32_e32 v155, vcc, 0, v147, vcc
	s_mov_b64 s[22:23], 0x2400
	global_store_dwordx4 v[154:155], v[64:67], off sc1
	global_store_dwordx4 v[148:149], v[60:63], off offset:16 sc1
	v_lshl_add_u64 v[148:149], v[146:147], 0, s[22:23]
	s_mov_b64 s[22:23], 0x2800
	global_store_dwordx4 v[154:155], v[56:59], off offset:1024 sc1
	global_store_dwordx4 v[148:149], v[48:51], off offset:16 sc1
	v_lshl_add_u64 v[148:149], v[146:147], 0, s[22:23]
	s_mov_b64 s[22:23], 0x2c00
	global_store_dwordx4 v[154:155], v[40:43], off offset:2048 sc1
	global_store_dwordx4 v[148:149], v[32:35], off offset:16 sc1
	v_lshl_add_u64 v[146:147], v[146:147], 0, s[22:23]
	global_store_dwordx4 v[154:155], v[24:27], off offset:3072 sc1
	global_store_dwordx4 v[146:147], v[16:19], off offset:16 sc1

; __device__ __forceinline__ unsigned xb_add(unsigned* p, unsigned v) { return __hip_atomic_fetch_add(p, v, __ATOMIC_RELAXED, __HIP_MEMORY_SCOPE_AGENT); }
; __device__ __forceinline__ void xcd_barrier(const XcdBarrier& b) {
;     ...
;         if (old + 1u == (gen + 1u) * nloc) {
;             __builtin_amdgcn_fence(__ATOMIC_RELEASE, XB_SCOPE);
;             asm volatile("s_waitcnt vmcnt(0)" ::: "memory");
;             const unsigned og = xb_add(&bar[XB_TOP], 1u);
.LBB0_810:
	s_andn2_saveexec_b64 s[6:7], s[6:7]
	s_cbranch_execz .LBB0_830
	s_mov_b64 s[6:7], exec
	s_nop 0
	s_waitcnt lgkmcnt(0)
	s_waitcnt vmcnt(0)
	v_mbcnt_lo_u32_b32 v0, s6, 0
	v_mbcnt_hi_u32_b32 v1, s7, v0
	v_cmp_eq_u32_e32 vcc, 0, v1
	s_and_saveexec_b64 s[8:9], vcc
	s_cbranch_execz .LBB0_813
	s_bcnt1_i32_b64 s6, s[6:7]
	v_mov_b32_e32 v0, s6
	v_mov_b32_e32 v4, 0x7000
	global_atomic_add v4, v4, v0, s[4:5] offset:1024 sc0

; __device__ __forceinline__ unsigned cvt_pk_bf16(float lo, float hi) { unsigned r; asm volatile("v_cvt_pk_bf16_f32 %0, %1, %2" : "=v"(r) : "v"(lo), "v"(hi)); return r; }
; #define PG8_BAR __builtin_amdgcn_s_barrier()
; template <class Epi, class Sched, bool ALIGN_EPI = false, bool SP2 = false, bool GATHER = false>
; __device__ __forceinline__ void gemm_phase(PG8_LAS unsigned char* lds, const Gemm g, const Sched& S, const Epi& E, const PG8_LAS int* rt = nullptr) {
;     ...
;         if constexpr (ALIGN_EPI) { if (wr == 1) PG8_BAR; }
;     __device__ __forceinline__ void operator()(const f32x4 (&acc)[2][2][4][2], const Unit& u, int wr, int wc, int fr, int fq) const {
;     ...
;             for (int m = 0; m < 4; ++m) { bf16_t* rowp = Yb + (size_t)(row0 + ai * HALF + m * 16) * 1024 + col0;
; #pragma unroll
;                 for (int bj = 0; bj < 2; ++bj) { const f32x4 v0 = acc[ai][bj][m][0], v1 = acc[ai][bj][m][1];
;                     u32x4 w; w.x = cvt_pk_bf16(v0[0], v0[1]); w.y = cvt_pk_bf16(v0[2], v0[3]); w.z = cvt_pk_bf16(v1[0], v1[1]); w.w = cvt_pk_bf16(v1[2], v1[3]);
;                     *(u32x4*)(rowp + bj * HALF) = w; } }
.LBB0_3874:
	v_lshl_add_u32 v150, s18, 8, v1
	s_lshl_b32 s9, s63, 8
	s_and_b32 s9, s9, 0x300
	v_ashrrev_i32_e32 v151, 31, v150
	v_or_b32_e32 v0, s9, v147
	v_lshlrev_b64 v[144:145], 11, v[150:151]
	v_lshl_add_u64 v[144:145], s[4:5], 0, v[144:145]
	v_lshlrev_b32_e32 v2, 1, v0
	v_lshl_add_u64 v[144:145], v[144:145], 0, v[2:3]
	v_cvt_pk_bf16_f32 v128, v128, v129
	v_cvt_pk_bf16_f32 v129, v130, v131
	v_cvt_pk_bf16_f32 v130, v124, v125
	v_cvt_pk_bf16_f32 v131, v126, v127
	global_store_dwordx4 v[144:145], v[128:131], off sc1
	v_cvt_pk_bf16_f32 v116, v116, v117
	v_cvt_pk_bf16_f32 v117, v118, v119
	v_cvt_pk_bf16_f32 v118, v108, v109
	v_or_b32_e32 v108, 16, v150
	v_ashrrev_i32_e32 v109, 31, v108
	v_lshlrev_b64 v[108:109], 11, v[108:109]
	v_lshl_add_u64 v[108:109], s[4:5], 0, v[108:109]
	v_cvt_pk_bf16_f32 v119, v110, v111
	global_store_dwordx4 v[144:145], v[116:119], off offset:256 sc1
	s_mov_b32 s9, 0x40000
	s_mov_b64 s[20:21], 0x40000
	v_lshl_add_u64 v[116:117], v[108:109], 0, v[2:3]
	v_cvt_pk_bf16_f32 v108, v120, v121
	v_cvt_pk_bf16_f32 v109, v122, v123
	v_cvt_pk_bf16_f32 v110, v112, v113
	v_cvt_pk_bf16_f32 v111, v114, v115
	global_store_dwordx4 v[116:117], v[108:111], off sc1
	v_cvt_pk_bf16_f32 v100, v100, v101
	v_cvt_pk_bf16_f32 v101, v102, v103
	v_cvt_pk_bf16_f32 v102, v92, v93
	v_or_b32_e32 v92, 32, v150
	v_ashrrev_i32_e32 v93, 31, v92
	v_lshlrev_b64 v[92:93], 11, v[92:93]
	v_lshl_add_u64 v[92:93], s[4:5], 0, v[92:93]
	v_cvt_pk_bf16_f32 v103, v94, v95
	global_store_dwordx4 v[116:117], v[100:103], off offset:256 sc1
	s_nop 1
	v_lshl_add_u64 v[100:101], v[92:93], 0, v[2:3]
	v_cvt_pk_bf16_f32 v92, v104, v105
	v_cvt_pk_bf16_f32 v93, v106, v107
	v_cvt_pk_bf16_f32 v94, v96, v97
	v_cvt_pk_bf16_f32 v95, v98, v99
	global_store_dwordx4 v[100:101], v[92:95], off sc1
	v_cvt_pk_bf16_f32 v84, v84, v85
	v_cvt_pk_bf16_f32 v85, v86, v87
	v_cvt_pk_bf16_f32 v86, v76, v77
	v_or_b32_e32 v76, 48, v150
	v_ashrrev_i32_e32 v77, 31, v76
	v_lshlrev_b64 v[76:77], 11, v[76:77]
	v_lshl_add_u64 v[76:77], s[4:5], 0, v[76:77]
	v_cvt_pk_bf16_f32 v87, v78, v79
	global_store_dwordx4 v[100:101], v[84:87], off offset:256 sc1
	s_nop 1
	v_lshl_add_u64 v[84:85], v[76:77], 0, v[2:3]
	v_cvt_pk_bf16_f32 v76, v88, v89
	v_cvt_pk_bf16_f32 v77, v90, v91
	v_cvt_pk_bf16_f32 v78, v80, v81
	v_cvt_pk_bf16_f32 v79, v82, v83
	global_store_dwordx4 v[84:85], v[76:79], off sc1
	v_cvt_pk_bf16_f32 v72, v72, v73
	v_cvt_pk_bf16_f32 v73, v74, v75
	v_cvt_pk_bf16_f32 v74, v68, v69
	v_cvt_pk_bf16_f32 v75, v70, v71
	global_store_dwordx4 v[84:85], v[72:75], off offset:256 sc1
	v_cvt_pk_bf16_f32 v64, v64, v65
	v_cvt_pk_bf16_f32 v65, v66, v67
	v_cvt_pk_bf16_f32 v66, v60, v61
	v_add_co_u32_e32 v60, vcc, s9, v144
	v_lshl_add_u64 v[68:69], v[144:145], 0, s[20:21]
	s_nop 0
	v_addc_co_u32_e32 v61, vcc, 0, v145, vcc
	s_mov_b32 s9, 0x48000
	v_cvt_pk_bf16_f32 v67, v62, v63
	global_store_dwordx4 v[60:61], v[64:67], off sc1
	v_cvt_pk_bf16_f32 v52, v52, v53
	v_cvt_pk_bf16_f32 v53, v54, v55
	v_cvt_pk_bf16_f32 v54, v44, v45
	v_cvt_pk_bf16_f32 v55, v46, v47
	global_store_dwordx4 v[68:69], v[52:55], off offset:256 sc1
	s_mov_b64 s[20:21], 0x48000
	v_cvt_pk_bf16_f32 v44, v56, v57
	v_cvt_pk_bf16_f32 v45, v58, v59
	v_cvt_pk_bf16_f32 v46, v48, v49
	v_add_co_u32_e32 v48, vcc, s9, v144
	v_lshl_add_u64 v[52:53], v[144:145], 0, s[20:21]
	s_nop 0
	v_addc_co_u32_e32 v49, vcc, 0, v145, vcc
	s_mov_b32 s9, 0x50000
	v_cvt_pk_bf16_f32 v47, v50, v51
	global_store_dwordx4 v[48:49], v[44:47], off sc1
	v_cvt_pk_bf16_f32 v36, v36, v37
	v_cvt_pk_bf16_f32 v37, v38, v39
	v_cvt_pk_bf16_f32 v38, v28, v29
	v_cvt_pk_bf16_f32 v39, v30, v31
	global_store_dwordx4 v[52:53], v[36:39], off offset:256 sc1
	s_mov_b64 s[20:21], 0x50000
	v_cvt_pk_bf16_f32 v28, v40, v41
	v_cvt_pk_bf16_f32 v29, v42, v43
	v_cvt_pk_bf16_f32 v30, v32, v33
	v_add_co_u32_e32 v32, vcc, s9, v144
	v_lshl_add_u64 v[36:37], v[144:145], 0, s[20:21]
	s_nop 0
	v_addc_co_u32_e32 v33, vcc, 0, v145, vcc
	s_mov_b32 s9, 0x58000
	v_cvt_pk_bf16_f32 v31, v34, v35
	global_store_dwordx4 v[32:33], v[28:31], off sc1
	v_cvt_pk_bf16_f32 v20, v20, v21
	v_cvt_pk_bf16_f32 v21, v22, v23
	v_cvt_pk_bf16_f32 v22, v12, v13
	v_cvt_pk_bf16_f32 v23, v14, v15
	global_store_dwordx4 v[36:37], v[20:23], off offset:256 sc1
	v_cvt_pk_bf16_f32 v12, v24, v25
	v_cvt_pk_bf16_f32 v13, v26, v27
	v_cvt_pk_bf16_f32 v14, v16, v17
	v_add_co_u32_e32 v16, vcc, s9, v144
	s_mov_b64 s[20:21], 0x58000
	s_nop 0
	v_addc_co_u32_e32 v17, vcc, 0, v145, vcc
	v_lshl_add_u64 v[20:21], v[144:145], 0, s[20:21]
	s_andn2_b64 vcc, exec, s[12:13]
	s_mov_b64 s[12:13], -1
	v_cvt_pk_bf16_f32 v15, v18, v19
	global_store_dwordx4 v[16:17], v[12:15], off sc1
	v_cvt_pk_bf16_f32 v8, v8, v9
	v_cvt_pk_bf16_f32 v9, v10, v11
	v_cvt_pk_bf16_f32 v10, v4, v5
	v_cvt_pk_bf16_f32 v11, v6, v7
	global_store_dwordx4 v[20:21], v[8:11], off offset:256 sc1
	s_cbranch_vccnz .LBB0_3867
	s_andn2_b64 vcc, exec, s[2:3]
	s_cbranch_vccnz .LBB0_3866
	s_barrier
	s_branch .LBB0_3866

; __device__ __forceinline__ unsigned xb_add(unsigned* p, unsigned v) { return __hip_atomic_fetch_add(p, v, __ATOMIC_RELAXED, __HIP_MEMORY_SCOPE_AGENT); }
; __device__ __forceinline__ void xcd_barrier(const XcdBarrier& b) {
;     ...
;         if (old + 1u == (gen + 1u) * nloc) {
;             __builtin_amdgcn_fence(__ATOMIC_RELEASE, XB_SCOPE);
;             asm volatile("s_waitcnt vmcnt(0)" ::: "memory");
;             const unsigned og = xb_add(&bar[XB_TOP], 1u);
.LBB0_3912:
	s_mov_b64 s[4:5], exec
	s_nop 0
	s_waitcnt lgkmcnt(0)
	s_waitcnt vmcnt(0)
	v_mbcnt_lo_u32_b32 v0, s4, 0
	v_mbcnt_hi_u32_b32 v1, s5, v0
	v_cmp_eq_u32_e32 vcc, 0, v1
	s_and_saveexec_b64 s[6:7], vcc
	s_cbranch_execz .LBB0_3914
	s_bcnt1_i32_b64 s4, s[4:5]
	v_mov_b32_e32 v0, s4
	v_mov_b32_e32 v4, 0x7000
	global_atomic_add v4, v4, v0, s[2:3] offset:1024 sc0
